# HGRN2 chunk loop: waves 0-1 issue the 16 intra-chunk score operand LDS reads right after the second barrier (data is final there), overlapping the scale/convert groups, so the score MFMA chain starts
# speedup vs baseline: 1.0107x; 1.0107x over previous
.LBB0_302:
	v_lshlrev_b32_e32 v139, 2, v101
	v_add_u32_e32 v6, s26, v139
	v_lshl_add_u32 v2, v6, 2, 0
	v_add_u32_e32 v7, 0x10400, v2
	s_waitcnt lgkmcnt(0)
	s_barrier
	ds_read_b128 v[2:5], v7
	ds_read_b128 v[34:37], v7 offset:32
	ds_read_b128 v[38:41], v7 offset:64
	ds_read_b128 v[42:45], v7 offset:96
	v_lshlrev_b32_e32 v8, 4, v100
	v_and_b32_e32 v9, 0xf0, v8
	v_lshl_add_u32 v10, v100, 8, s27
	v_lshlrev_b32_e32 v6, 1, v6
	s_andn2_b64 vcc, exec, s[42:43]
	s_nop 0
	s_cbranch_vccz .Lhg_qpath
	s_waitcnt lgkmcnt(3)
	v_mul_f32_e32 v2, v84, v2
	v_mul_f32_e32 v3, v85, v3
	v_cvt_pk_bf16_f32 v2, v2, v3
	v_mul_f32_e32 v3, v86, v4
	v_mul_f32_e32 v4, v87, v5
	v_cvt_pk_bf16_f32 v3, v3, v4
	v_xad_u32 v4, v6, v9, v10
	ds_write_b64 v4, v[2:3] offset:32768
	s_waitcnt lgkmcnt(3)
	v_mul_f32_e32 v2, v88, v34
	v_mul_f32_e32 v3, v89, v35
	v_cvt_pk_bf16_f32 v2, v2, v3
	v_mul_f32_e32 v3, v90, v36
	v_mul_f32_e32 v4, v91, v37
	v_cvt_pk_bf16_f32 v3, v3, v4
	v_add_u32_e32 v4, 16, v6
	v_xad_u32 v4, v4, v9, v10
	ds_write_b64 v4, v[2:3] offset:32768
	s_waitcnt lgkmcnt(3)
	v_mul_f32_e32 v2, v92, v38
	v_mul_f32_e32 v3, v93, v39
	v_cvt_pk_bf16_f32 v2, v2, v3
	v_mul_f32_e32 v3, v94, v40
	v_mul_f32_e32 v4, v95, v41
	v_cvt_pk_bf16_f32 v3, v3, v4
	v_add_u32_e32 v4, 32, v6
	v_xad_u32 v4, v4, v9, v10
	ds_write_b64 v4, v[2:3] offset:32768
	s_waitcnt lgkmcnt(3)
	v_mul_f32_e32 v2, v96, v42
	v_mul_f32_e32 v3, v97, v43
	v_cvt_pk_bf16_f32 v2, v2, v3
	v_mul_f32_e32 v3, v98, v44
	v_mul_f32_e32 v4, v99, v45
	v_cvt_pk_bf16_f32 v3, v3, v4
	v_add_u32_e32 v4, 48, v6
	v_xad_u32 v4, v4, v9, v10
	ds_write_b64 v4, v[2:3] offset:32768
	v_lshlrev_b32_e32 v2, 3, v100
	v_and_b32_e32 v4, 0xc0, v8
	v_lshl_add_u32 v3, v101, 8, v2
	v_and_or_b32 v2, v2, 24, v4
	v_lshlrev_b32_e32 v4, 1, v100
	v_and_b32_e32 v4, 32, v4
	v_and_b32_e32 v3, 0x100, v3
	v_or3_b32 v2, v2, v4, v3
	s_waitcnt lgkmcnt(0)
	s_branch .Lhg_bar3
.Lhg_qpath:
	ds_read_b128 v[182:185], v105 offset:8192
	ds_read_b128 v[140:143], v105
	ds_read_b128 v[186:189], v106 offset:8192
	ds_read_b128 v[144:147], v106
	ds_read_b128 v[190:193], v107 offset:8192
	ds_read_b128 v[148:151], v107
	ds_read_b128 v[194:197], v108 offset:8192
	ds_read_b128 v[74:77], v108
	s_waitcnt lgkmcnt(11)
	v_mul_f32_e32 v2, v84, v2
	v_mul_f32_e32 v3, v85, v3
	v_cvt_pk_bf16_f32 v2, v2, v3
	v_mul_f32_e32 v3, v86, v4
	v_mul_f32_e32 v4, v87, v5
	v_cvt_pk_bf16_f32 v3, v3, v4
	v_xad_u32 v4, v6, v9, v10
	ds_write_b64 v4, v[2:3] offset:32768
	s_waitcnt lgkmcnt(11)
	v_mul_f32_e32 v2, v88, v34
	v_mul_f32_e32 v3, v89, v35
	v_cvt_pk_bf16_f32 v2, v2, v3
	v_mul_f32_e32 v3, v90, v36
	v_mul_f32_e32 v4, v91, v37
	v_cvt_pk_bf16_f32 v3, v3, v4
	v_add_u32_e32 v4, 16, v6
	v_xad_u32 v4, v4, v9, v10
	ds_write_b64 v4, v[2:3] offset:32768
	s_waitcnt lgkmcnt(11)
	v_mul_f32_e32 v2, v92, v38
	v_mul_f32_e32 v3, v93, v39
	v_cvt_pk_bf16_f32 v2, v2, v3
	v_mul_f32_e32 v3, v94, v40
	v_mul_f32_e32 v4, v95, v41
	v_cvt_pk_bf16_f32 v3, v3, v4
	v_add_u32_e32 v4, 32, v6
	v_xad_u32 v4, v4, v9, v10
	ds_write_b64 v4, v[2:3] offset:32768
	s_waitcnt lgkmcnt(11)
	v_mul_f32_e32 v2, v96, v42
	v_mul_f32_e32 v3, v97, v43
	v_cvt_pk_bf16_f32 v2, v2, v3
	v_mul_f32_e32 v3, v98, v44
	v_mul_f32_e32 v4, v99, v45
	v_cvt_pk_bf16_f32 v3, v3, v4
	v_add_u32_e32 v4, 48, v6
	v_xad_u32 v4, v4, v9, v10
	ds_write_b64 v4, v[2:3] offset:32768
	ds_read_b128 v[198:201], v109 offset:8192
	ds_read_b128 v[78:81], v109
	ds_read_b128 v[202:205], v110 offset:8192
	ds_read_b128 v[156:159], v110
	ds_read_b128 v[234:237], v111 offset:8192
	ds_read_b128 v[160:163], v111
	ds_read_b128 v[238:241], v112 offset:8192
	ds_read_b128 v[152:155], v112
	v_lshlrev_b32_e32 v2, 3, v100
	v_and_b32_e32 v4, 0xc0, v8
	v_lshl_add_u32 v3, v101, 8, v2
	v_and_or_b32 v2, v2, 24, v4
	v_lshlrev_b32_e32 v4, 1, v100
	v_and_b32_e32 v4, 32, v4
	v_and_b32_e32 v3, 0x100, v3
	v_or3_b32 v2, v2, v4, v3
	s_waitcnt lgkmcnt(8)
.Lhg_bar3:
	s_barrier
	v_add_u32_e32 v3, s28, v2
	ds_read_b64_tr_b16 v[70:71], v3 offset:0
	ds_read_b64_tr_b16 v[72:73], v3 offset:0x800
	ds_read_b64_tr_b16 v[66:67], v3 offset:0x1000
	ds_read_b64_tr_b16 v[68:69], v3 offset:0x1800
	v_add_u32_e32 v6, s29, v2
	ds_read_b64_tr_b16 v[2:3], v6 offset:0
	ds_read_b64_tr_b16 v[4:5], v6 offset:0x800
	ds_read_b64_tr_b16 v[18:19], v6 offset:0x1000
	ds_read_b64_tr_b16 v[20:21], v6 offset:0x1800
	s_waitcnt lgkmcnt(0)
	v_lshlrev_b32_e32 v6, 4, v101
	v_add_u32_e32 v22, s33, v6
	v_add_u32_e32 v23, s46, v6
	v_mfma_f32_32x32x16_bf16 v[2:17], v[2:5], v[70:73], 0
	ds_read_b128 v[34:37], v22
	ds_read_b128 v[38:41], v22 offset:32
	ds_read_b128 v[58:61], v23
	ds_read_b128 v[54:57], v23 offset:32
	ds_read_b128 v[42:45], v22 offset:64
	ds_read_b128 v[50:53], v23 offset:64
	ds_read_b128 v[46:49], v22 offset:96
	ds_read_b128 v[62:65], v23 offset:96
	s_andn2_b64 vcc, exec, s[42:43]
	v_mfma_f32_32x32x16_bf16 v[2:17], v[18:21], v[66:69], v[2:17]
	s_cbranch_vccnz .LBB0_295
	v_cmp_le_i32_e32 vcc, v139, v100
	v_or_b32_e32 v172, 2, v139
	v_or_b32_e32 v173, 3, v139
	v_add_u32_e32 v174, 8, v139
	v_add_u32_e32 v175, 9, v139
	v_add_u32_e32 v176, 10, v139
	v_add_u32_e32 v177, 11, v139
	v_add_u32_e32 v178, 24, v139
	v_add_u32_e32 v179, 25, v139
	v_add_u32_e32 v180, 26, v139
	s_lshl_b32 s56, s7, 5
	s_cmp_gt_i32 s7, 7
	s_cselect_b32 s7, s90, 0xff
	s_sub_i32 s7, s7, s56
	s_and_b64 s[76:77], s[10:11], exec
	s_cselect_b32 s7, s56, s7
	s_add_i32 s76, s7, s3
	s_ashr_i32 s77, s76, 31
	s_lshl_b64 s[76:77], s[76:77], 11
	s_add_u32 s76, s47, s76
	s_addc_u32 s77, s52, s77
	v_add_u32_e32 v164, 16, v139
	v_add_u32_e32 v165, 17, v139
	v_add_u32_e32 v166, 18, v139
	v_add_u32_e32 v167, 19, v139
	s_waitcnt lgkmcnt(14)
	v_mfma_f32_32x32x16_bf16 v[18:33], v[182:185], v[140:143], 0
	s_waitcnt lgkmcnt(12)
	v_mfma_f32_32x32x16_bf16 v[18:33], v[186:189], v[144:147], v[18:33]
	s_waitcnt lgkmcnt(10)
	v_mfma_f32_32x32x16_bf16 v[18:33], v[190:193], v[148:151], v[18:33]
	s_waitcnt lgkmcnt(8)
	v_mfma_f32_32x32x16_bf16 v[18:33], v[194:197], v[74:77], v[18:33]
	s_waitcnt lgkmcnt(6)
	v_mfma_f32_32x32x16_bf16 v[18:33], v[198:201], v[78:81], v[18:33]
	s_waitcnt lgkmcnt(4)
	v_mfma_f32_32x32x16_bf16 v[18:33], v[202:205], v[156:159], v[18:33]
	s_waitcnt lgkmcnt(2)
	v_mfma_f32_32x32x16_bf16 v[18:33], v[234:237], v[160:163], v[18:33]
	s_waitcnt lgkmcnt(0)
	v_mfma_f32_32x32x16_bf16 v[18:33], v[238:241], v[152:155], v[18:33]
	v_add_u32_e32 v242, s27, v105
	ds_read_b128 v[182:185], v242 offset:32768
	v_add_u32_e32 v242, s27, v106
	ds_read_b128 v[186:189], v242 offset:32768
	v_add_u32_e32 v242, s27, v107
	ds_read_b128 v[190:193], v242 offset:32768
	v_add_u32_e32 v242, s27, v108
	ds_read_b128 v[194:197], v242 offset:32768
	v_add_u32_e32 v242, s27, v109
	ds_read_b128 v[198:201], v242 offset:32768
	v_add_u32_e32 v242, s27, v110
	ds_read_b128 v[202:205], v242 offset:32768
	v_add_u32_e32 v242, s27, v111
	ds_read_b128 v[234:237], v242 offset:32768
	v_add_u32_e32 v242, s27, v112
	ds_read_b128 v[238:241], v242 offset:32768
	v_cndmask_b32_e32 v18, 0, v18, vcc
	v_cmp_lt_i32_e32 vcc, v139, v100
	v_add_u32_e32 v139, 27, v139
	s_nop 0
	v_cndmask_b32_e32 v19, 0, v19, vcc
	v_cmp_le_i32_e32 vcc, v172, v100
	v_cvt_pk_bf16_f32 v18, v18, v19
	s_nop 1
	v_cndmask_b32_e32 v20, 0, v20, vcc
	v_cmp_le_i32_e32 vcc, v173, v100
	s_nop 1
	v_cndmask_b32_e32 v21, 0, v21, vcc
	v_cmp_le_i32_e32 vcc, v174, v100
	v_cvt_pk_bf16_f32 v19, v20, v21
	s_nop 1
	v_cndmask_b32_e32 v22, 0, v22, vcc
	v_cmp_le_i32_e32 vcc, v175, v100
	s_nop 1
	v_cndmask_b32_e32 v23, 0, v23, vcc
	v_cmp_le_i32_e32 vcc, v176, v100
	v_cvt_pk_bf16_f32 v20, v22, v23
	s_nop 0
	v_permlane32_swap_b32_e32 v18, v20
	v_cndmask_b32_e32 v24, 0, v24, vcc
	v_cmp_le_i32_e32 vcc, v177, v100
	s_nop 1
	v_cndmask_b32_e32 v25, 0, v25, vcc
	v_cmp_le_i32_e32 vcc, v164, v100
	v_cvt_pk_bf16_f32 v21, v24, v25
	s_nop 0
	v_permlane32_swap_b32_e32 v19, v21
	v_cndmask_b32_e32 v26, 0, v26, vcc
	v_cmp_le_i32_e32 vcc, v165, v100
	s_nop 1
	v_cndmask_b32_e32 v27, 0, v27, vcc
	v_cmp_le_i32_e32 vcc, v166, v100
	v_cvt_pk_bf16_f32 v164, v26, v27
	s_nop 1
	v_cndmask_b32_e32 v28, 0, v28, vcc
	v_cmp_le_i32_e32 vcc, v167, v100
	s_nop 1
	v_cndmask_b32_e32 v29, 0, v29, vcc
	v_cmp_le_i32_e32 vcc, v178, v100
	v_cvt_pk_bf16_f32 v165, v28, v29
	s_nop 1
	v_cndmask_b32_e32 v30, 0, v30, vcc
	v_cmp_le_i32_e32 vcc, v179, v100
	s_nop 1
	v_cndmask_b32_e32 v31, 0, v31, vcc
	v_cmp_le_i32_e32 vcc, v180, v100
	v_cvt_pk_bf16_f32 v166, v30, v31
	s_nop 0
	v_permlane32_swap_b32_e32 v164, v166
	v_cndmask_b32_e32 v32, 0, v32, vcc
	v_cmp_le_i32_e32 vcc, v139, v100
	v_add_u32_e32 v139, s27, v110
	s_nop 0
	v_cndmask_b32_e32 v33, 0, v33, vcc
	v_cvt_pk_bf16_f32 v167, v32, v33
	v_mfma_f32_32x32x16_bf16 v[18:33], v[18:21], v[70:73], 0
	v_permlane32_swap_b32_e32 v165, v167
	s_nop 1
	v_mfma_f32_32x32x16_bf16 v[18:33], v[164:167], v[66:69], v[18:33]
	s_waitcnt lgkmcnt(0)
	v_mfma_f32_32x32x16_bf16 v[18:33], v[140:143], v[182:185], v[18:33]
	v_mul_lo_u32 v140, s53, v101
	v_ashrrev_i32_e32 v141, 31, v140
	v_ashrrev_i32_e32 v101, 31, v100
	v_mfma_f32_32x32x16_bf16 v[18:33], v[144:147], v[186:189], v[18:33]
	v_mfma_f32_32x32x16_bf16 v[18:33], v[148:151], v[190:193], v[18:33]
	v_mfma_f32_32x32x16_bf16 v[18:33], v[74:77], v[194:197], v[18:33]
	v_mfma_f32_32x32x16_bf16 v[18:33], v[78:81], v[198:201], v[18:33]
	v_lshl_add_u64 v[66:67], v[140:141], 2, s[76:77]
	v_lshl_add_u64 v[74:75], v[100:101], 2, v[66:67]
	v_lshl_add_u64 v[76:77], s[62:63], 2, v[74:75]
	v_lshl_add_u64 v[78:79], v[76:77], 0, s[86:87]
	v_lshl_add_u64 v[80:81], v[78:79], 0, s[86:87]
	v_lshl_add_u64 v[100:101], v[80:81], 0, s[50:51]
	v_mfma_f32_32x32x16_bf16 v[18:33], v[156:159], v[202:205], v[18:33]
	v_lshl_add_u64 v[140:141], v[100:101], 0, s[86:87]
	v_mfma_f32_32x32x16_bf16 v[18:33], v[160:163], v[234:237], v[18:33]
	v_lshl_add_u64 v[66:67], v[140:141], 0, s[86:87]
	v_lshl_add_u64 v[68:69], v[66:67], 0, s[86:87]
	v_lshl_add_u64 v[142:143], v[68:69], 0, s[50:51]
	v_lshl_add_u64 v[144:145], v[142:143], 0, s[86:87]
	v_lshl_add_u64 v[146:147], v[144:145], 0, s[86:87]
	v_lshl_add_u64 v[148:149], v[146:147], 0, s[86:87]
	v_lshl_add_u64 v[150:151], v[148:149], 0, s[50:51]
	v_mfma_f32_32x32x16_bf16 v[18:33], v[152:155], v[238:241], v[18:33]
	s_nop 11
	global_store_dword v[74:75], v18, off
	global_store_dword v[76:77], v19, off
	global_store_dword v[78:79], v20, off
	global_store_dword v[80:81], v21, off
	global_store_dword v[100:101], v22, off
	global_store_dword v[140:141], v23, off
	global_store_dword v[66:67], v24, off
	global_store_dword v[68:69], v25, off
	global_store_dword v[142:143], v26, off
	global_store_dword v[144:145], v27, off
	global_store_dword v[146:147], v28, off
	global_store_dword v[148:149], v29, off
	global_store_dword v[150:151], v30, off
	v_lshl_add_u64 v[18:19], v[150:151], 0, s[86:87]
	global_store_dword v[18:19], v31, off
	v_lshl_add_u64 v[18:19], v[18:19], 0, s[86:87]
	global_store_dword v[18:19], v32, off
	v_lshl_add_u64 v[18:19], v[18:19], 0, s[86:87]
	global_store_dword v[18:19], v33, off
	s_branch .LBB0_295
